# qkv: A-tile DMA for the next super-step issued early, right after all waves have read their A fragments
# speedup vs baseline: 1.0053x; 1.0053x over previous
_Z14k_qkv_temporalPKDF16_S0_PKfPDF16_S3_S3_PfPi:
	s_load_dwordx4 s[36:39], s[0:1], 0x0
	s_load_dwordx2 s[40:41], s[0:1], 0x10
	s_load_dwordx4 s[8:11], s[0:1], 0x30
	s_and_b32 s3, s2, 7
	s_mul_i32 s3, s3, 0x71
	s_lshr_b32 s4, s2, 3
	s_add_u32 s3, s3, s4
	s_and_b32 s22, s3, 7
	s_lshr_b32 s16, s3, 3
	s_mul_i32 s16, s16, 14
	v_lshrrev_b32_e32 v1, 6, v0
	v_and_b32_e32 v92, 15, v0
	v_bfe_u32 v90, v0, 4, 2
	v_lshlrev_b32_e32 v95, 2, v90
	v_lshl_or_b32 v91, v1, 5, v95
	v_bfe_u32 v162, v0, 3, 3
	v_and_b32_e32 v163, 7, v0
	v_lshrrev_b32_e32 v110, 1, v162
	v_and_b32_e32 v111, 1, v1
	v_lshl_or_b32 v110, v111, 2, v110
	v_xor_b32_e32 v110, v163, v110
	v_lshlrev_b32_e32 v110, 4, v110
	v_lshl_or_b32 v111, v1, 3, v162
	s_mov_b32 s42, 0x12492493
	s_movk_i32 s43, 0x627
	s_movk_i32 s44, 0x628
	v_add_u32_e32 v112, 0, v111
	v_min_u32_e32 v112, 0x7d, v112
	v_mul_hi_u32 v113, v112, s42
	v_mul_u32_u24_e32 v114, 14, v113
	v_sub_u32_e32 v114, v112, v114
	v_add_u32_e32 v114, s16, v114
	v_min_u32_e32 v114, s43, v114
	v_mad_u32_u24 v114, v113, s44, v114
	v_lshl_or_b32 v100, v114, 10, v110
	v_add_u32_e32 v112, 32, v111
	v_min_u32_e32 v112, 0x7d, v112
	v_mul_hi_u32 v113, v112, s42
	v_mul_u32_u24_e32 v114, 14, v113
	v_sub_u32_e32 v114, v112, v114
	v_add_u32_e32 v114, s16, v114
	v_min_u32_e32 v114, s43, v114
	v_mad_u32_u24 v114, v113, s44, v114
	v_lshl_or_b32 v101, v114, 10, v110
	v_add_u32_e32 v112, 64, v111
	v_min_u32_e32 v112, 0x7d, v112
	v_mul_hi_u32 v113, v112, s42
	v_mul_u32_u24_e32 v114, 14, v113
	v_sub_u32_e32 v114, v112, v114
	v_add_u32_e32 v114, s16, v114
	v_min_u32_e32 v114, s43, v114
	v_mad_u32_u24 v114, v113, s44, v114
	v_lshl_or_b32 v102, v114, 10, v110
	v_add_u32_e32 v112, 96, v111
	v_min_u32_e32 v112, 0x7d, v112
	v_mul_hi_u32 v113, v112, s42
	v_mul_u32_u24_e32 v114, 14, v113
	v_sub_u32_e32 v114, v112, v114
	v_add_u32_e32 v114, s16, v114
	v_min_u32_e32 v114, s43, v114
	v_mad_u32_u24 v114, v113, s44, v114
	v_lshl_or_b32 v103, v114, 10, v110
	s_lshl_b32 s45, s22, 6
	v_add_u32_e32 v112, s45, v111
	v_lshl_or_b32 v112, v112, 10, v110
	v_mov_b32_e32 v104, v112
	v_add_u32_e32 v105, 0x8000, v112
	v_add_u32_e32 v106, 0x80000, v112
	v_add_u32_e32 v107, 0x88000, v112
	v_add_u32_e32 v108, 0x100000, v112
	v_add_u32_e32 v109, 0x108000, v112
	v_lshlrev_b32_e32 v113, 10, v1
	s_nop 0
	v_readfirstlane_b32 s24, v113
	s_add_u32 s25, s24, 0x1000
	s_add_u32 s26, s24, 0x2000
	s_add_u32 s27, s24, 0x3000
	s_add_u32 s28, s24, 0x4000
	s_add_u32 s29, s24, 0x5000
	s_add_u32 s30, s24, 0x6000
	s_add_u32 s31, s24, 0x7000
	s_add_u32 s32, s24, 0x8000
	s_add_u32 s33, s24, 0x9000
	s_add_u32 s46, s24, 0xa000
	s_add_u32 s47, s25, 0xa000
	s_add_u32 s48, s26, 0xa000
	s_add_u32 s49, s27, 0xa000
	s_add_u32 s50, s28, 0xa000
	s_add_u32 s51, s29, 0xa000
	s_add_u32 s52, s30, 0xa000
	s_add_u32 s53, s31, 0xa000
	s_add_u32 s54, s32, 0xa000
	s_add_u32 s55, s33, 0xa000
	v_lshrrev_b32_e32 v113, 1, v92
	v_xor_b32_e32 v113, v90, v113
	v_lshlrev_b32_e32 v113, 4, v113
	v_lshl_or_b32 v160, v92, 7, v113
	v_xor_b32_e32 v161, 64, v160
	v_lshlrev_b32_e32 v114, 12, v1
	v_add_u32_e32 v158, v114, v160
	v_xor_b32_e32 v159, 64, v158
	v_lshl_add_u32 v114, s22, 6, v92
	v_lshlrev_b32_e32 v114, 2, v114
	v_add_u32_e32 v115, 0x1000, v114
	s_waitcnt lgkmcnt(0)
	global_load_dword v116, v114, s[40:41] offset:0
	global_load_dword v117, v114, s[40:41] offset:64
	global_load_dword v118, v114, s[40:41] offset:128
	global_load_dword v119, v114, s[40:41] offset:192
	global_load_dword v120, v114, s[40:41] offset:2048
	global_load_dword v121, v114, s[40:41] offset:2112
	global_load_dword v122, v114, s[40:41] offset:2176
	global_load_dword v123, v114, s[40:41] offset:2240
	global_load_dword v124, v115, s[40:41] offset:0
	global_load_dword v125, v115, s[40:41] offset:64
	global_load_dword v126, v115, s[40:41] offset:128
	global_load_dword v127, v115, s[40:41] offset:192
	s_mov_b32 m0, s24
	s_nop 0
	global_load_lds_dwordx4 v100, s[36:37]
	s_mov_b32 m0, s25
	s_nop 0
	global_load_lds_dwordx4 v101, s[36:37]
	s_mov_b32 m0, s26
	s_nop 0
	global_load_lds_dwordx4 v102, s[36:37]
	s_mov_b32 m0, s27
	s_nop 0
	global_load_lds_dwordx4 v103, s[36:37]
	s_mov_b32 m0, s28
	s_nop 0
	global_load_lds_dwordx4 v104, s[38:39]
	s_mov_b32 m0, s29
	s_nop 0
	global_load_lds_dwordx4 v105, s[38:39]
	s_mov_b32 m0, s30
	s_nop 0
	global_load_lds_dwordx4 v106, s[38:39]
	s_mov_b32 m0, s31
	s_nop 0
	global_load_lds_dwordx4 v107, s[38:39]
	s_mov_b32 m0, s32
	s_nop 0
	global_load_lds_dwordx4 v108, s[38:39]
	s_mov_b32 m0, s33
	s_nop 0
	global_load_lds_dwordx4 v109, s[38:39]
	s_add_u32 s36, s36, 0x80
	s_addc_u32 s37, s37, 0
	s_add_u32 s38, s38, 0x80
	s_addc_u32 s39, s39, 0
	s_waitcnt vmcnt(10)
	v_mov_b32_e32 v164, v116
	v_mov_b32_e32 v165, v116
	v_mov_b32_e32 v166, v116
	v_mov_b32_e32 v167, v116
	v_mov_b32_e32 v62, v116
	v_mov_b32_e32 v63, v116
	v_mov_b32_e32 v64, v116
	v_mov_b32_e32 v65, v116
	v_mov_b32_e32 v86, v117
	v_mov_b32_e32 v87, v117
	v_mov_b32_e32 v88, v117
	v_mov_b32_e32 v89, v117
	v_mov_b32_e32 v58, v117
	v_mov_b32_e32 v59, v117
	v_mov_b32_e32 v60, v117
	v_mov_b32_e32 v61, v117
	v_mov_b32_e32 v96, v118
	v_mov_b32_e32 v97, v118
	v_mov_b32_e32 v98, v118
	v_mov_b32_e32 v99, v118
	v_mov_b32_e32 v54, v118
	v_mov_b32_e32 v55, v118
	v_mov_b32_e32 v56, v118
	v_mov_b32_e32 v57, v118
	v_mov_b32_e32 v82, v119
	v_mov_b32_e32 v83, v119
	v_mov_b32_e32 v84, v119
	v_mov_b32_e32 v85, v119
	v_mov_b32_e32 v50, v119
	v_mov_b32_e32 v51, v119
	v_mov_b32_e32 v52, v119
	v_mov_b32_e32 v53, v119
	v_mov_b32_e32 v78, v120
	v_mov_b32_e32 v79, v120
	v_mov_b32_e32 v80, v120
	v_mov_b32_e32 v81, v120
	v_mov_b32_e32 v46, v120
	v_mov_b32_e32 v47, v120
	v_mov_b32_e32 v48, v120
	v_mov_b32_e32 v49, v120
	v_mov_b32_e32 v74, v121
	v_mov_b32_e32 v75, v121
	v_mov_b32_e32 v76, v121
	v_mov_b32_e32 v77, v121
	v_mov_b32_e32 v42, v121
	v_mov_b32_e32 v43, v121
	v_mov_b32_e32 v44, v121
	v_mov_b32_e32 v45, v121
	v_mov_b32_e32 v70, v122
	v_mov_b32_e32 v71, v122
	v_mov_b32_e32 v72, v122
	v_mov_b32_e32 v73, v122
	v_mov_b32_e32 v38, v122
	v_mov_b32_e32 v39, v122
	v_mov_b32_e32 v40, v122
	v_mov_b32_e32 v41, v122
	v_mov_b32_e32 v66, v123
	v_mov_b32_e32 v67, v123
	v_mov_b32_e32 v68, v123
	v_mov_b32_e32 v69, v123
	v_mov_b32_e32 v34, v123
	v_mov_b32_e32 v35, v123
	v_mov_b32_e32 v36, v123
	v_mov_b32_e32 v37, v123
	v_mov_b32_e32 v18, v124
	v_mov_b32_e32 v19, v124
	v_mov_b32_e32 v20, v124
	v_mov_b32_e32 v21, v124
	v_mov_b32_e32 v2, v124
	v_mov_b32_e32 v3, v124
	v_mov_b32_e32 v4, v124
	v_mov_b32_e32 v5, v124
	v_mov_b32_e32 v26, v125
	v_mov_b32_e32 v27, v125
	v_mov_b32_e32 v28, v125
	v_mov_b32_e32 v29, v125
	v_mov_b32_e32 v10, v125
	v_mov_b32_e32 v11, v125
	v_mov_b32_e32 v12, v125
	v_mov_b32_e32 v13, v125
	v_mov_b32_e32 v22, v126
	v_mov_b32_e32 v23, v126
	v_mov_b32_e32 v24, v126
	v_mov_b32_e32 v25, v126
	v_mov_b32_e32 v6, v126
	v_mov_b32_e32 v7, v126
	v_mov_b32_e32 v8, v126
	v_mov_b32_e32 v9, v126
	v_mov_b32_e32 v30, v127
	v_mov_b32_e32 v31, v127
	v_mov_b32_e32 v32, v127
	v_mov_b32_e32 v33, v127
	v_mov_b32_e32 v14, v127
	v_mov_b32_e32 v15, v127
	v_mov_b32_e32 v16, v127
	v_mov_b32_e32 v17, v127
	s_waitcnt vmcnt(0)
	s_barrier
	ds_read_b128 v[110:113], v158 offset:0
	ds_read_b128 v[114:117], v158 offset:2048
	ds_read_b128 v[118:121], v159 offset:0
	ds_read_b128 v[122:125], v159 offset:2048
	ds_read_b128 v[126:129], v160 offset:16384
	ds_read_b128 v[130:133], v160 offset:18432
	ds_read_b128 v[134:137], v160 offset:20480
	ds_read_b128 v[138:141], v160 offset:22528
	ds_read_b128 v[142:145], v160 offset:24576
	ds_read_b128 v[146:149], v160 offset:26624
	ds_read_b128 v[150:153], v160 offset:28672
	ds_read_b128 v[154:157], v160 offset:30720
	s_waitcnt lgkmcnt(7)
	v_mfma_f32_16x16x32_f16 v[164:167], v[110:113], v[126:129], v[164:167]
	v_mfma_f32_16x16x32_f16 v[62:65], v[114:117], v[126:129], v[62:65]
	ds_read_b128 v[126:129], v160 offset:32768
	s_waitcnt lgkmcnt(7)
	v_mfma_f32_16x16x32_f16 v[86:89], v[110:113], v[130:133], v[86:89]
	v_mfma_f32_16x16x32_f16 v[58:61], v[114:117], v[130:133], v[58:61]
	ds_read_b128 v[130:133], v160 offset:34816
	s_waitcnt lgkmcnt(10)
	s_barrier
	s_mov_b32 m0, s24
	s_nop 0
	global_load_lds_dwordx4 v100, s[36:37]
	s_mov_b32 m0, s25
	s_nop 0
	global_load_lds_dwordx4 v101, s[36:37]
	s_mov_b32 m0, s26
	s_nop 0
	global_load_lds_dwordx4 v102, s[36:37]
	s_mov_b32 m0, s27
	s_nop 0
	global_load_lds_dwordx4 v103, s[36:37]
	s_add_u32 s36, s36, 0x80
	s_addc_u32 s37, s37, 0
	s_waitcnt lgkmcnt(7)
	v_mfma_f32_16x16x32_f16 v[96:99], v[110:113], v[134:137], v[96:99]
	v_mfma_f32_16x16x32_f16 v[54:57], v[114:117], v[134:137], v[54:57]
	ds_read_b128 v[134:137], v160 offset:36864
	s_waitcnt lgkmcnt(7)
	v_mfma_f32_16x16x32_f16 v[82:85], v[110:113], v[138:141], v[82:85]
	v_mfma_f32_16x16x32_f16 v[50:53], v[114:117], v[138:141], v[50:53]
	ds_read_b128 v[138:141], v160 offset:38912
	s_waitcnt lgkmcnt(7)
	v_mfma_f32_16x16x32_f16 v[78:81], v[110:113], v[142:145], v[78:81]
	v_mfma_f32_16x16x32_f16 v[46:49], v[114:117], v[142:145], v[46:49]
	ds_read_b128 v[142:145], v161 offset:16384
	s_waitcnt lgkmcnt(7)
	v_mfma_f32_16x16x32_f16 v[74:77], v[110:113], v[146:149], v[74:77]
	v_mfma_f32_16x16x32_f16 v[42:45], v[114:117], v[146:149], v[42:45]
	ds_read_b128 v[146:149], v161 offset:18432
	s_waitcnt lgkmcnt(7)
	v_mfma_f32_16x16x32_f16 v[70:73], v[110:113], v[150:153], v[70:73]
	v_mfma_f32_16x16x32_f16 v[38:41], v[114:117], v[150:153], v[38:41]
	ds_read_b128 v[150:153], v161 offset:20480
	s_waitcnt lgkmcnt(7)
	v_mfma_f32_16x16x32_f16 v[66:69], v[110:113], v[154:157], v[66:69]
	v_mfma_f32_16x16x32_f16 v[34:37], v[114:117], v[154:157], v[34:37]
	ds_read_b128 v[154:157], v161 offset:22528
	s_waitcnt lgkmcnt(7)
	v_mfma_f32_16x16x32_f16 v[18:21], v[110:113], v[126:129], v[18:21]
	v_mfma_f32_16x16x32_f16 v[2:5], v[114:117], v[126:129], v[2:5]
	ds_read_b128 v[126:129], v161 offset:24576
	s_waitcnt lgkmcnt(7)
	v_mfma_f32_16x16x32_f16 v[26:29], v[110:113], v[130:133], v[26:29]
	v_mfma_f32_16x16x32_f16 v[10:13], v[114:117], v[130:133], v[10:13]
	ds_read_b128 v[130:133], v161 offset:26624
	s_waitcnt lgkmcnt(7)
	v_mfma_f32_16x16x32_f16 v[22:25], v[110:113], v[134:137], v[22:25]
	v_mfma_f32_16x16x32_f16 v[6:9], v[114:117], v[134:137], v[6:9]
	ds_read_b128 v[134:137], v161 offset:28672
	s_waitcnt lgkmcnt(7)
	v_mfma_f32_16x16x32_f16 v[30:33], v[110:113], v[138:141], v[30:33]
	v_mfma_f32_16x16x32_f16 v[14:17], v[114:117], v[138:141], v[14:17]
	ds_read_b128 v[138:141], v161 offset:30720
	s_waitcnt lgkmcnt(7)
	v_mfma_f32_16x16x32_f16 v[164:167], v[118:121], v[142:145], v[164:167]
	v_mfma_f32_16x16x32_f16 v[62:65], v[122:125], v[142:145], v[62:65]
	ds_read_b128 v[142:145], v161 offset:32768
	s_waitcnt lgkmcnt(7)
	v_mfma_f32_16x16x32_f16 v[86:89], v[118:121], v[146:149], v[86:89]
	v_mfma_f32_16x16x32_f16 v[58:61], v[122:125], v[146:149], v[58:61]
	ds_read_b128 v[146:149], v161 offset:34816
	s_waitcnt lgkmcnt(7)
	v_mfma_f32_16x16x32_f16 v[96:99], v[118:121], v[150:153], v[96:99]
	v_mfma_f32_16x16x32_f16 v[54:57], v[122:125], v[150:153], v[54:57]
	ds_read_b128 v[150:153], v161 offset:36864
	s_waitcnt lgkmcnt(7)
	v_mfma_f32_16x16x32_f16 v[82:85], v[118:121], v[154:157], v[82:85]
	v_mfma_f32_16x16x32_f16 v[50:53], v[122:125], v[154:157], v[50:53]
	ds_read_b128 v[154:157], v161 offset:38912
	s_waitcnt lgkmcnt(0)
	s_barrier
	s_mov_b32 m0, s28
	s_nop 0
	global_load_lds_dwordx4 v104, s[38:39]
	s_mov_b32 m0, s29
	s_nop 0
	global_load_lds_dwordx4 v105, s[38:39]
	s_mov_b32 m0, s30
	s_nop 0
	global_load_lds_dwordx4 v106, s[38:39]
	s_mov_b32 m0, s31
	s_nop 0
	global_load_lds_dwordx4 v107, s[38:39]
	s_mov_b32 m0, s32
	s_nop 0
	global_load_lds_dwordx4 v108, s[38:39]
	s_mov_b32 m0, s33
	s_nop 0
	global_load_lds_dwordx4 v109, s[38:39]
	s_add_u32 s38, s38, 0x80
	s_addc_u32 s39, s39, 0
	s_waitcnt lgkmcnt(7)
	v_mfma_f32_16x16x32_f16 v[78:81], v[118:121], v[126:129], v[78:81]
	v_mfma_f32_16x16x32_f16 v[46:49], v[122:125], v[126:129], v[46:49]
	s_waitcnt lgkmcnt(6)
	v_mfma_f32_16x16x32_f16 v[74:77], v[118:121], v[130:133], v[74:77]
	v_mfma_f32_16x16x32_f16 v[42:45], v[122:125], v[130:133], v[42:45]
	s_waitcnt lgkmcnt(5)
	v_mfma_f32_16x16x32_f16 v[70:73], v[118:121], v[134:137], v[70:73]
	v_mfma_f32_16x16x32_f16 v[38:41], v[122:125], v[134:137], v[38:41]
	s_waitcnt lgkmcnt(4)
	v_mfma_f32_16x16x32_f16 v[66:69], v[118:121], v[138:141], v[66:69]
	v_mfma_f32_16x16x32_f16 v[34:37], v[122:125], v[138:141], v[34:37]
	s_waitcnt lgkmcnt(3)
	v_mfma_f32_16x16x32_f16 v[18:21], v[118:121], v[142:145], v[18:21]
	v_mfma_f32_16x16x32_f16 v[2:5], v[122:125], v[142:145], v[2:5]
	s_waitcnt lgkmcnt(2)
	v_mfma_f32_16x16x32_f16 v[26:29], v[118:121], v[146:149], v[26:29]
	v_mfma_f32_16x16x32_f16 v[10:13], v[122:125], v[146:149], v[10:13]
	s_waitcnt lgkmcnt(1)
	v_mfma_f32_16x16x32_f16 v[22:25], v[118:121], v[150:153], v[22:25]
	v_mfma_f32_16x16x32_f16 v[6:9], v[122:125], v[150:153], v[6:9]
	s_waitcnt lgkmcnt(0)
	v_mfma_f32_16x16x32_f16 v[30:33], v[118:121], v[154:157], v[30:33]
	v_mfma_f32_16x16x32_f16 v[14:17], v[122:125], v[154:157], v[14:17]
	s_waitcnt vmcnt(0)
	s_barrier
	ds_read_b128 v[110:113], v158 offset:0
	ds_read_b128 v[114:117], v158 offset:2048
	ds_read_b128 v[118:121], v159 offset:0
	ds_read_b128 v[122:125], v159 offset:2048
	ds_read_b128 v[126:129], v160 offset:16384
	ds_read_b128 v[130:133], v160 offset:18432
	ds_read_b128 v[134:137], v160 offset:20480
	ds_read_b128 v[138:141], v160 offset:22528
	ds_read_b128 v[142:145], v160 offset:24576
	ds_read_b128 v[146:149], v160 offset:26624
	ds_read_b128 v[150:153], v160 offset:28672
	ds_read_b128 v[154:157], v160 offset:30720
	s_waitcnt lgkmcnt(7)
	v_mfma_f32_16x16x32_f16 v[164:167], v[110:113], v[126:129], v[164:167]
	v_mfma_f32_16x16x32_f16 v[62:65], v[114:117], v[126:129], v[62:65]
	ds_read_b128 v[126:129], v160 offset:32768
	s_waitcnt lgkmcnt(7)
	v_mfma_f32_16x16x32_f16 v[86:89], v[110:113], v[130:133], v[86:89]
	v_mfma_f32_16x16x32_f16 v[58:61], v[114:117], v[130:133], v[58:61]
	ds_read_b128 v[130:133], v160 offset:34816
	s_waitcnt lgkmcnt(10)
	s_barrier
	s_mov_b32 m0, s24
	s_nop 0
	global_load_lds_dwordx4 v100, s[36:37]
	s_mov_b32 m0, s25
	s_nop 0
	global_load_lds_dwordx4 v101, s[36:37]
	s_mov_b32 m0, s26
	s_nop 0
	global_load_lds_dwordx4 v102, s[36:37]
	s_mov_b32 m0, s27
	s_nop 0
	global_load_lds_dwordx4 v103, s[36:37]
	s_add_u32 s36, s36, 0x80
	s_addc_u32 s37, s37, 0
	s_waitcnt lgkmcnt(7)
	v_mfma_f32_16x16x32_f16 v[96:99], v[110:113], v[134:137], v[96:99]
	v_mfma_f32_16x16x32_f16 v[54:57], v[114:117], v[134:137], v[54:57]
	ds_read_b128 v[134:137], v160 offset:36864
	s_waitcnt lgkmcnt(7)
	v_mfma_f32_16x16x32_f16 v[82:85], v[110:113], v[138:141], v[82:85]
	v_mfma_f32_16x16x32_f16 v[50:53], v[114:117], v[138:141], v[50:53]
	ds_read_b128 v[138:141], v160 offset:38912
	s_waitcnt lgkmcnt(7)
	v_mfma_f32_16x16x32_f16 v[78:81], v[110:113], v[142:145], v[78:81]
	v_mfma_f32_16x16x32_f16 v[46:49], v[114:117], v[142:145], v[46:49]
	ds_read_b128 v[142:145], v161 offset:16384
	s_waitcnt lgkmcnt(7)
	v_mfma_f32_16x16x32_f16 v[74:77], v[110:113], v[146:149], v[74:77]
	v_mfma_f32_16x16x32_f16 v[42:45], v[114:117], v[146:149], v[42:45]
	ds_read_b128 v[146:149], v161 offset:18432
	s_waitcnt lgkmcnt(7)
	v_mfma_f32_16x16x32_f16 v[70:73], v[110:113], v[150:153], v[70:73]
	v_mfma_f32_16x16x32_f16 v[38:41], v[114:117], v[150:153], v[38:41]
	ds_read_b128 v[150:153], v161 offset:20480
	s_waitcnt lgkmcnt(7)
	v_mfma_f32_16x16x32_f16 v[66:69], v[110:113], v[154:157], v[66:69]
	v_mfma_f32_16x16x32_f16 v[34:37], v[114:117], v[154:157], v[34:37]
	ds_read_b128 v[154:157], v161 offset:22528
	s_waitcnt lgkmcnt(7)
	v_mfma_f32_16x16x32_f16 v[18:21], v[110:113], v[126:129], v[18:21]
	v_mfma_f32_16x16x32_f16 v[2:5], v[114:117], v[126:129], v[2:5]
	ds_read_b128 v[126:129], v161 offset:24576
	s_waitcnt lgkmcnt(7)
	v_mfma_f32_16x16x32_f16 v[26:29], v[110:113], v[130:133], v[26:29]
	v_mfma_f32_16x16x32_f16 v[10:13], v[114:117], v[130:133], v[10:13]
	ds_read_b128 v[130:133], v161 offset:26624
	s_waitcnt lgkmcnt(7)
	v_mfma_f32_16x16x32_f16 v[22:25], v[110:113], v[134:137], v[22:25]
	v_mfma_f32_16x16x32_f16 v[6:9], v[114:117], v[134:137], v[6:9]
	ds_read_b128 v[134:137], v161 offset:28672
	s_waitcnt lgkmcnt(7)
	v_mfma_f32_16x16x32_f16 v[30:33], v[110:113], v[138:141], v[30:33]
	v_mfma_f32_16x16x32_f16 v[14:17], v[114:117], v[138:141], v[14:17]
	ds_read_b128 v[138:141], v161 offset:30720
	s_waitcnt lgkmcnt(7)
	v_mfma_f32_16x16x32_f16 v[164:167], v[118:121], v[142:145], v[164:167]
	v_mfma_f32_16x16x32_f16 v[62:65], v[122:125], v[142:145], v[62:65]
	ds_read_b128 v[142:145], v161 offset:32768
	s_waitcnt lgkmcnt(7)
	v_mfma_f32_16x16x32_f16 v[86:89], v[118:121], v[146:149], v[86:89]
	v_mfma_f32_16x16x32_f16 v[58:61], v[122:125], v[146:149], v[58:61]
	ds_read_b128 v[146:149], v161 offset:34816
	s_waitcnt lgkmcnt(7)
	v_mfma_f32_16x16x32_f16 v[96:99], v[118:121], v[150:153], v[96:99]
	v_mfma_f32_16x16x32_f16 v[54:57], v[122:125], v[150:153], v[54:57]
	ds_read_b128 v[150:153], v161 offset:36864
	s_waitcnt lgkmcnt(7)
	v_mfma_f32_16x16x32_f16 v[82:85], v[118:121], v[154:157], v[82:85]
	v_mfma_f32_16x16x32_f16 v[50:53], v[122:125], v[154:157], v[50:53]
	ds_read_b128 v[154:157], v161 offset:38912
	s_waitcnt lgkmcnt(0)
	s_barrier
	s_mov_b32 m0, s28
	s_nop 0
	global_load_lds_dwordx4 v104, s[38:39]
	s_mov_b32 m0, s29
	s_nop 0
	global_load_lds_dwordx4 v105, s[38:39]
	s_mov_b32 m0, s30
	s_nop 0
	global_load_lds_dwordx4 v106, s[38:39]
	s_mov_b32 m0, s31
	s_nop 0
	global_load_lds_dwordx4 v107, s[38:39]
	s_mov_b32 m0, s32
	s_nop 0
	global_load_lds_dwordx4 v108, s[38:39]
	s_mov_b32 m0, s33
	s_nop 0
	global_load_lds_dwordx4 v109, s[38:39]
	s_add_u32 s38, s38, 0x80
	s_addc_u32 s39, s39, 0
	s_waitcnt lgkmcnt(7)
	v_mfma_f32_16x16x32_f16 v[78:81], v[118:121], v[126:129], v[78:81]
	v_mfma_f32_16x16x32_f16 v[46:49], v[122:125], v[126:129], v[46:49]
	s_waitcnt lgkmcnt(6)
	v_mfma_f32_16x16x32_f16 v[74:77], v[118:121], v[130:133], v[74:77]
	v_mfma_f32_16x16x32_f16 v[42:45], v[122:125], v[130:133], v[42:45]
	s_waitcnt lgkmcnt(5)
	v_mfma_f32_16x16x32_f16 v[70:73], v[118:121], v[134:137], v[70:73]
	v_mfma_f32_16x16x32_f16 v[38:41], v[122:125], v[134:137], v[38:41]
	s_waitcnt lgkmcnt(4)
	v_mfma_f32_16x16x32_f16 v[66:69], v[118:121], v[138:141], v[66:69]
	v_mfma_f32_16x16x32_f16 v[34:37], v[122:125], v[138:141], v[34:37]
	s_waitcnt lgkmcnt(3)
	v_mfma_f32_16x16x32_f16 v[18:21], v[118:121], v[142:145], v[18:21]
	v_mfma_f32_16x16x32_f16 v[2:5], v[122:125], v[142:145], v[2:5]
	s_waitcnt lgkmcnt(2)
	v_mfma_f32_16x16x32_f16 v[26:29], v[118:121], v[146:149], v[26:29]
	v_mfma_f32_16x16x32_f16 v[10:13], v[122:125], v[146:149], v[10:13]
	s_waitcnt lgkmcnt(1)
	v_mfma_f32_16x16x32_f16 v[22:25], v[118:121], v[150:153], v[22:25]
	v_mfma_f32_16x16x32_f16 v[6:9], v[122:125], v[150:153], v[6:9]
	s_waitcnt lgkmcnt(0)
	v_mfma_f32_16x16x32_f16 v[30:33], v[118:121], v[154:157], v[30:33]
	v_mfma_f32_16x16x32_f16 v[14:17], v[122:125], v[154:157], v[14:17]
	s_waitcnt vmcnt(0)
	s_barrier
	ds_read_b128 v[110:113], v158 offset:0
	ds_read_b128 v[114:117], v158 offset:2048
	ds_read_b128 v[118:121], v159 offset:0
	ds_read_b128 v[122:125], v159 offset:2048
	ds_read_b128 v[126:129], v160 offset:16384
	ds_read_b128 v[130:133], v160 offset:18432
	ds_read_b128 v[134:137], v160 offset:20480
	ds_read_b128 v[138:141], v160 offset:22528
	ds_read_b128 v[142:145], v160 offset:24576
	ds_read_b128 v[146:149], v160 offset:26624
	ds_read_b128 v[150:153], v160 offset:28672
	ds_read_b128 v[154:157], v160 offset:30720
	s_waitcnt lgkmcnt(7)
	v_mfma_f32_16x16x32_f16 v[164:167], v[110:113], v[126:129], v[164:167]
	v_mfma_f32_16x16x32_f16 v[62:65], v[114:117], v[126:129], v[62:65]
	ds_read_b128 v[126:129], v160 offset:32768
	s_waitcnt lgkmcnt(7)
	v_mfma_f32_16x16x32_f16 v[86:89], v[110:113], v[130:133], v[86:89]
	v_mfma_f32_16x16x32_f16 v[58:61], v[114:117], v[130:133], v[58:61]
	ds_read_b128 v[130:133], v160 offset:34816
	s_waitcnt lgkmcnt(10)
	s_barrier
	s_mov_b32 m0, s24
	s_nop 0
	global_load_lds_dwordx4 v100, s[36:37]
	s_mov_b32 m0, s25
	s_nop 0
	global_load_lds_dwordx4 v101, s[36:37]
	s_mov_b32 m0, s26
	s_nop 0
	global_load_lds_dwordx4 v102, s[36:37]
	s_mov_b32 m0, s27
	s_nop 0
	global_load_lds_dwordx4 v103, s[36:37]
	s_add_u32 s36, s36, 0x80
	s_addc_u32 s37, s37, 0
	s_waitcnt lgkmcnt(7)
	v_mfma_f32_16x16x32_f16 v[96:99], v[110:113], v[134:137], v[96:99]
	v_mfma_f32_16x16x32_f16 v[54:57], v[114:117], v[134:137], v[54:57]
	ds_read_b128 v[134:137], v160 offset:36864
	s_waitcnt lgkmcnt(7)
	v_mfma_f32_16x16x32_f16 v[82:85], v[110:113], v[138:141], v[82:85]
	v_mfma_f32_16x16x32_f16 v[50:53], v[114:117], v[138:141], v[50:53]
	ds_read_b128 v[138:141], v160 offset:38912
	s_waitcnt lgkmcnt(7)
	v_mfma_f32_16x16x32_f16 v[78:81], v[110:113], v[142:145], v[78:81]
	v_mfma_f32_16x16x32_f16 v[46:49], v[114:117], v[142:145], v[46:49]
	ds_read_b128 v[142:145], v161 offset:16384
	s_waitcnt lgkmcnt(7)
	v_mfma_f32_16x16x32_f16 v[74:77], v[110:113], v[146:149], v[74:77]
	v_mfma_f32_16x16x32_f16 v[42:45], v[114:117], v[146:149], v[42:45]
	ds_read_b128 v[146:149], v161 offset:18432
	s_waitcnt lgkmcnt(7)
	v_mfma_f32_16x16x32_f16 v[70:73], v[110:113], v[150:153], v[70:73]
	v_mfma_f32_16x16x32_f16 v[38:41], v[114:117], v[150:153], v[38:41]
	ds_read_b128 v[150:153], v161 offset:20480
	s_waitcnt lgkmcnt(7)
	v_mfma_f32_16x16x32_f16 v[66:69], v[110:113], v[154:157], v[66:69]
	v_mfma_f32_16x16x32_f16 v[34:37], v[114:117], v[154:157], v[34:37]
	ds_read_b128 v[154:157], v161 offset:22528
	s_waitcnt lgkmcnt(7)
	v_mfma_f32_16x16x32_f16 v[18:21], v[110:113], v[126:129], v[18:21]
	v_mfma_f32_16x16x32_f16 v[2:5], v[114:117], v[126:129], v[2:5]
	ds_read_b128 v[126:129], v161 offset:24576
	s_waitcnt lgkmcnt(7)
	v_mfma_f32_16x16x32_f16 v[26:29], v[110:113], v[130:133], v[26:29]
	v_mfma_f32_16x16x32_f16 v[10:13], v[114:117], v[130:133], v[10:13]
	ds_read_b128 v[130:133], v161 offset:26624
	s_waitcnt lgkmcnt(7)
	v_mfma_f32_16x16x32_f16 v[22:25], v[110:113], v[134:137], v[22:25]
	v_mfma_f32_16x16x32_f16 v[6:9], v[114:117], v[134:137], v[6:9]
	ds_read_b128 v[134:137], v161 offset:28672
	s_waitcnt lgkmcnt(7)
	v_mfma_f32_16x16x32_f16 v[30:33], v[110:113], v[138:141], v[30:33]
	v_mfma_f32_16x16x32_f16 v[14:17], v[114:117], v[138:141], v[14:17]
	ds_read_b128 v[138:141], v161 offset:30720
	s_waitcnt lgkmcnt(7)
	v_mfma_f32_16x16x32_f16 v[164:167], v[118:121], v[142:145], v[164:167]
	v_mfma_f32_16x16x32_f16 v[62:65], v[122:125], v[142:145], v[62:65]
	ds_read_b128 v[142:145], v161 offset:32768
	s_waitcnt lgkmcnt(7)
	v_mfma_f32_16x16x32_f16 v[86:89], v[118:121], v[146:149], v[86:89]
	v_mfma_f32_16x16x32_f16 v[58:61], v[122:125], v[146:149], v[58:61]
	ds_read_b128 v[146:149], v161 offset:34816
	s_waitcnt lgkmcnt(7)
	v_mfma_f32_16x16x32_f16 v[96:99], v[118:121], v[150:153], v[96:99]
	v_mfma_f32_16x16x32_f16 v[54:57], v[122:125], v[150:153], v[54:57]
	ds_read_b128 v[150:153], v161 offset:36864
	s_waitcnt lgkmcnt(7)
	v_mfma_f32_16x16x32_f16 v[82:85], v[118:121], v[154:157], v[82:85]
	v_mfma_f32_16x16x32_f16 v[50:53], v[122:125], v[154:157], v[50:53]
	ds_read_b128 v[154:157], v161 offset:38912
	s_waitcnt lgkmcnt(0)
	s_barrier
	s_mov_b32 m0, s28
	s_nop 0
	global_load_lds_dwordx4 v104, s[38:39]
	s_mov_b32 m0, s29
	s_nop 0
	global_load_lds_dwordx4 v105, s[38:39]
	s_mov_b32 m0, s30
	s_nop 0
	global_load_lds_dwordx4 v106, s[38:39]
	s_mov_b32 m0, s31
	s_nop 0
	global_load_lds_dwordx4 v107, s[38:39]
	s_mov_b32 m0, s32
	s_nop 0
	global_load_lds_dwordx4 v108, s[38:39]
	s_mov_b32 m0, s33
	s_nop 0
	global_load_lds_dwordx4 v109, s[38:39]
	s_add_u32 s38, s38, 0x80
	s_addc_u32 s39, s39, 0
	s_waitcnt lgkmcnt(7)
	v_mfma_f32_16x16x32_f16 v[78:81], v[118:121], v[126:129], v[78:81]
	v_mfma_f32_16x16x32_f16 v[46:49], v[122:125], v[126:129], v[46:49]
	s_waitcnt lgkmcnt(6)
	v_mfma_f32_16x16x32_f16 v[74:77], v[118:121], v[130:133], v[74:77]
	v_mfma_f32_16x16x32_f16 v[42:45], v[122:125], v[130:133], v[42:45]
	s_waitcnt lgkmcnt(5)
	v_mfma_f32_16x16x32_f16 v[70:73], v[118:121], v[134:137], v[70:73]
	v_mfma_f32_16x16x32_f16 v[38:41], v[122:125], v[134:137], v[38:41]
	s_waitcnt lgkmcnt(4)
	v_mfma_f32_16x16x32_f16 v[66:69], v[118:121], v[138:141], v[66:69]
	v_mfma_f32_16x16x32_f16 v[34:37], v[122:125], v[138:141], v[34:37]
	s_waitcnt lgkmcnt(3)
	v_mfma_f32_16x16x32_f16 v[18:21], v[118:121], v[142:145], v[18:21]
	v_mfma_f32_16x16x32_f16 v[2:5], v[122:125], v[142:145], v[2:5]
	s_waitcnt lgkmcnt(2)
	v_mfma_f32_16x16x32_f16 v[26:29], v[118:121], v[146:149], v[26:29]
	v_mfma_f32_16x16x32_f16 v[10:13], v[122:125], v[146:149], v[10:13]
	s_waitcnt lgkmcnt(1)
	v_mfma_f32_16x16x32_f16 v[22:25], v[118:121], v[150:153], v[22:25]
	v_mfma_f32_16x16x32_f16 v[6:9], v[122:125], v[150:153], v[6:9]
	s_waitcnt lgkmcnt(0)
	v_mfma_f32_16x16x32_f16 v[30:33], v[118:121], v[154:157], v[30:33]
	v_mfma_f32_16x16x32_f16 v[14:17], v[122:125], v[154:157], v[14:17]
	s_waitcnt vmcnt(0)
	s_barrier
	ds_read_b128 v[110:113], v158 offset:0
	ds_read_b128 v[114:117], v158 offset:2048
	ds_read_b128 v[118:121], v159 offset:0
	ds_read_b128 v[122:125], v159 offset:2048
	ds_read_b128 v[126:129], v160 offset:16384
	ds_read_b128 v[130:133], v160 offset:18432
	ds_read_b128 v[134:137], v160 offset:20480
	ds_read_b128 v[138:141], v160 offset:22528
	ds_read_b128 v[142:145], v160 offset:24576
	ds_read_b128 v[146:149], v160 offset:26624
	ds_read_b128 v[150:153], v160 offset:28672
	ds_read_b128 v[154:157], v160 offset:30720
	s_waitcnt lgkmcnt(7)
	v_mfma_f32_16x16x32_f16 v[164:167], v[110:113], v[126:129], v[164:167]
	v_mfma_f32_16x16x32_f16 v[62:65], v[114:117], v[126:129], v[62:65]
	ds_read_b128 v[126:129], v160 offset:32768
	s_waitcnt lgkmcnt(7)
	v_mfma_f32_16x16x32_f16 v[86:89], v[110:113], v[130:133], v[86:89]
	v_mfma_f32_16x16x32_f16 v[58:61], v[114:117], v[130:133], v[58:61]
	ds_read_b128 v[130:133], v160 offset:34816
	s_waitcnt lgkmcnt(10)
	s_barrier
	s_mov_b32 m0, s24
	s_nop 0
	global_load_lds_dwordx4 v100, s[36:37]
	s_mov_b32 m0, s25
	s_nop 0
	global_load_lds_dwordx4 v101, s[36:37]
	s_mov_b32 m0, s26
	s_nop 0
	global_load_lds_dwordx4 v102, s[36:37]
	s_mov_b32 m0, s27
	s_nop 0
	global_load_lds_dwordx4 v103, s[36:37]
	s_add_u32 s36, s36, 0x80
	s_addc_u32 s37, s37, 0
	s_waitcnt lgkmcnt(7)
	v_mfma_f32_16x16x32_f16 v[96:99], v[110:113], v[134:137], v[96:99]
	v_mfma_f32_16x16x32_f16 v[54:57], v[114:117], v[134:137], v[54:57]
	ds_read_b128 v[134:137], v160 offset:36864
	s_waitcnt lgkmcnt(7)
	v_mfma_f32_16x16x32_f16 v[82:85], v[110:113], v[138:141], v[82:85]
	v_mfma_f32_16x16x32_f16 v[50:53], v[114:117], v[138:141], v[50:53]
	ds_read_b128 v[138:141], v160 offset:38912
	s_waitcnt lgkmcnt(7)
	v_mfma_f32_16x16x32_f16 v[78:81], v[110:113], v[142:145], v[78:81]
	v_mfma_f32_16x16x32_f16 v[46:49], v[114:117], v[142:145], v[46:49]
	ds_read_b128 v[142:145], v161 offset:16384
	s_waitcnt lgkmcnt(7)
	v_mfma_f32_16x16x32_f16 v[74:77], v[110:113], v[146:149], v[74:77]
	v_mfma_f32_16x16x32_f16 v[42:45], v[114:117], v[146:149], v[42:45]
	ds_read_b128 v[146:149], v161 offset:18432
	s_waitcnt lgkmcnt(7)
	v_mfma_f32_16x16x32_f16 v[70:73], v[110:113], v[150:153], v[70:73]
	v_mfma_f32_16x16x32_f16 v[38:41], v[114:117], v[150:153], v[38:41]
	ds_read_b128 v[150:153], v161 offset:20480
	s_waitcnt lgkmcnt(7)
	v_mfma_f32_16x16x32_f16 v[66:69], v[110:113], v[154:157], v[66:69]
	v_mfma_f32_16x16x32_f16 v[34:37], v[114:117], v[154:157], v[34:37]
	ds_read_b128 v[154:157], v161 offset:22528
	s_waitcnt lgkmcnt(7)
	v_mfma_f32_16x16x32_f16 v[18:21], v[110:113], v[126:129], v[18:21]
	v_mfma_f32_16x16x32_f16 v[2:5], v[114:117], v[126:129], v[2:5]
	ds_read_b128 v[126:129], v161 offset:24576
	s_waitcnt lgkmcnt(7)
	v_mfma_f32_16x16x32_f16 v[26:29], v[110:113], v[130:133], v[26:29]
	v_mfma_f32_16x16x32_f16 v[10:13], v[114:117], v[130:133], v[10:13]
	ds_read_b128 v[130:133], v161 offset:26624
	s_waitcnt lgkmcnt(7)
	v_mfma_f32_16x16x32_f16 v[22:25], v[110:113], v[134:137], v[22:25]
	v_mfma_f32_16x16x32_f16 v[6:9], v[114:117], v[134:137], v[6:9]
	ds_read_b128 v[134:137], v161 offset:28672
	s_waitcnt lgkmcnt(7)
	v_mfma_f32_16x16x32_f16 v[30:33], v[110:113], v[138:141], v[30:33]
	v_mfma_f32_16x16x32_f16 v[14:17], v[114:117], v[138:141], v[14:17]
	ds_read_b128 v[138:141], v161 offset:30720
	s_waitcnt lgkmcnt(7)
	v_mfma_f32_16x16x32_f16 v[164:167], v[118:121], v[142:145], v[164:167]
	v_mfma_f32_16x16x32_f16 v[62:65], v[122:125], v[142:145], v[62:65]
	ds_read_b128 v[142:145], v161 offset:32768
	s_waitcnt lgkmcnt(7)
	v_mfma_f32_16x16x32_f16 v[86:89], v[118:121], v[146:149], v[86:89]
	v_mfma_f32_16x16x32_f16 v[58:61], v[122:125], v[146:149], v[58:61]
	ds_read_b128 v[146:149], v161 offset:34816
	s_waitcnt lgkmcnt(7)
	v_mfma_f32_16x16x32_f16 v[96:99], v[118:121], v[150:153], v[96:99]
	v_mfma_f32_16x16x32_f16 v[54:57], v[122:125], v[150:153], v[54:57]
	ds_read_b128 v[150:153], v161 offset:36864
	s_waitcnt lgkmcnt(7)
	v_mfma_f32_16x16x32_f16 v[82:85], v[118:121], v[154:157], v[82:85]
	v_mfma_f32_16x16x32_f16 v[50:53], v[122:125], v[154:157], v[50:53]
	ds_read_b128 v[154:157], v161 offset:38912
	s_waitcnt lgkmcnt(0)
	s_barrier
	s_mov_b32 m0, s28
	s_nop 0
	global_load_lds_dwordx4 v104, s[38:39]
	s_mov_b32 m0, s29
	s_nop 0
	global_load_lds_dwordx4 v105, s[38:39]
	s_mov_b32 m0, s30
	s_nop 0
	global_load_lds_dwordx4 v106, s[38:39]
	s_mov_b32 m0, s31
	s_nop 0
	global_load_lds_dwordx4 v107, s[38:39]
	s_mov_b32 m0, s32
	s_nop 0
	global_load_lds_dwordx4 v108, s[38:39]
	s_mov_b32 m0, s33
	s_nop 0
	global_load_lds_dwordx4 v109, s[38:39]
	s_add_u32 s38, s38, 0x80
	s_addc_u32 s39, s39, 0
	s_waitcnt lgkmcnt(7)
	v_mfma_f32_16x16x32_f16 v[78:81], v[118:121], v[126:129], v[78:81]
	v_mfma_f32_16x16x32_f16 v[46:49], v[122:125], v[126:129], v[46:49]
	s_waitcnt lgkmcnt(6)
	v_mfma_f32_16x16x32_f16 v[74:77], v[118:121], v[130:133], v[74:77]
	v_mfma_f32_16x16x32_f16 v[42:45], v[122:125], v[130:133], v[42:45]
	s_waitcnt lgkmcnt(5)
	v_mfma_f32_16x16x32_f16 v[70:73], v[118:121], v[134:137], v[70:73]
	v_mfma_f32_16x16x32_f16 v[38:41], v[122:125], v[134:137], v[38:41]
	s_waitcnt lgkmcnt(4)
	v_mfma_f32_16x16x32_f16 v[66:69], v[118:121], v[138:141], v[66:69]
	v_mfma_f32_16x16x32_f16 v[34:37], v[122:125], v[138:141], v[34:37]
	s_waitcnt lgkmcnt(3)
	v_mfma_f32_16x16x32_f16 v[18:21], v[118:121], v[142:145], v[18:21]
	v_mfma_f32_16x16x32_f16 v[2:5], v[122:125], v[142:145], v[2:5]
	s_waitcnt lgkmcnt(2)
	v_mfma_f32_16x16x32_f16 v[26:29], v[118:121], v[146:149], v[26:29]
	v_mfma_f32_16x16x32_f16 v[10:13], v[122:125], v[146:149], v[10:13]
	s_waitcnt lgkmcnt(1)
	v_mfma_f32_16x16x32_f16 v[22:25], v[118:121], v[150:153], v[22:25]
	v_mfma_f32_16x16x32_f16 v[6:9], v[122:125], v[150:153], v[6:9]
	s_waitcnt lgkmcnt(0)
	v_mfma_f32_16x16x32_f16 v[30:33], v[118:121], v[154:157], v[30:33]
	v_mfma_f32_16x16x32_f16 v[14:17], v[122:125], v[154:157], v[14:17]
	s_waitcnt vmcnt(0)
	s_barrier
	ds_read_b128 v[110:113], v158 offset:0
	ds_read_b128 v[114:117], v158 offset:2048
	ds_read_b128 v[118:121], v159 offset:0
	ds_read_b128 v[122:125], v159 offset:2048
	ds_read_b128 v[126:129], v160 offset:16384
	ds_read_b128 v[130:133], v160 offset:18432
	ds_read_b128 v[134:137], v160 offset:20480
	ds_read_b128 v[138:141], v160 offset:22528
	ds_read_b128 v[142:145], v160 offset:24576
	ds_read_b128 v[146:149], v160 offset:26624
	ds_read_b128 v[150:153], v160 offset:28672
	ds_read_b128 v[154:157], v160 offset:30720
	s_waitcnt lgkmcnt(7)
	v_mfma_f32_16x16x32_f16 v[164:167], v[110:113], v[126:129], v[164:167]
	v_mfma_f32_16x16x32_f16 v[62:65], v[114:117], v[126:129], v[62:65]
	ds_read_b128 v[126:129], v160 offset:32768
	s_waitcnt lgkmcnt(7)
	v_mfma_f32_16x16x32_f16 v[86:89], v[110:113], v[130:133], v[86:89]
	v_mfma_f32_16x16x32_f16 v[58:61], v[114:117], v[130:133], v[58:61]
	ds_read_b128 v[130:133], v160 offset:34816
	s_waitcnt lgkmcnt(10)
	s_barrier
	s_mov_b32 m0, s24
	s_nop 0
	global_load_lds_dwordx4 v100, s[36:37]
	s_mov_b32 m0, s25
	s_nop 0
	global_load_lds_dwordx4 v101, s[36:37]
	s_mov_b32 m0, s26
	s_nop 0
	global_load_lds_dwordx4 v102, s[36:37]
	s_mov_b32 m0, s27
	s_nop 0
	global_load_lds_dwordx4 v103, s[36:37]
	s_add_u32 s36, s36, 0x80
	s_addc_u32 s37, s37, 0
	s_waitcnt lgkmcnt(7)
	v_mfma_f32_16x16x32_f16 v[96:99], v[110:113], v[134:137], v[96:99]
	v_mfma_f32_16x16x32_f16 v[54:57], v[114:117], v[134:137], v[54:57]
	ds_read_b128 v[134:137], v160 offset:36864
	s_waitcnt lgkmcnt(7)
	v_mfma_f32_16x16x32_f16 v[82:85], v[110:113], v[138:141], v[82:85]
	v_mfma_f32_16x16x32_f16 v[50:53], v[114:117], v[138:141], v[50:53]
	ds_read_b128 v[138:141], v160 offset:38912
	s_waitcnt lgkmcnt(7)
	v_mfma_f32_16x16x32_f16 v[78:81], v[110:113], v[142:145], v[78:81]
	v_mfma_f32_16x16x32_f16 v[46:49], v[114:117], v[142:145], v[46:49]
	ds_read_b128 v[142:145], v161 offset:16384
	s_waitcnt lgkmcnt(7)
	v_mfma_f32_16x16x32_f16 v[74:77], v[110:113], v[146:149], v[74:77]
	v_mfma_f32_16x16x32_f16 v[42:45], v[114:117], v[146:149], v[42:45]
	ds_read_b128 v[146:149], v161 offset:18432
	s_waitcnt lgkmcnt(7)
	v_mfma_f32_16x16x32_f16 v[70:73], v[110:113], v[150:153], v[70:73]
	v_mfma_f32_16x16x32_f16 v[38:41], v[114:117], v[150:153], v[38:41]
	ds_read_b128 v[150:153], v161 offset:20480
	s_waitcnt lgkmcnt(7)
	v_mfma_f32_16x16x32_f16 v[66:69], v[110:113], v[154:157], v[66:69]
	v_mfma_f32_16x16x32_f16 v[34:37], v[114:117], v[154:157], v[34:37]
	ds_read_b128 v[154:157], v161 offset:22528
	s_waitcnt lgkmcnt(7)
	v_mfma_f32_16x16x32_f16 v[18:21], v[110:113], v[126:129], v[18:21]
	v_mfma_f32_16x16x32_f16 v[2:5], v[114:117], v[126:129], v[2:5]
	ds_read_b128 v[126:129], v161 offset:24576
	s_waitcnt lgkmcnt(7)
	v_mfma_f32_16x16x32_f16 v[26:29], v[110:113], v[130:133], v[26:29]
	v_mfma_f32_16x16x32_f16 v[10:13], v[114:117], v[130:133], v[10:13]
	ds_read_b128 v[130:133], v161 offset:26624
	s_waitcnt lgkmcnt(7)
	v_mfma_f32_16x16x32_f16 v[22:25], v[110:113], v[134:137], v[22:25]
	v_mfma_f32_16x16x32_f16 v[6:9], v[114:117], v[134:137], v[6:9]
	ds_read_b128 v[134:137], v161 offset:28672
	s_waitcnt lgkmcnt(7)
	v_mfma_f32_16x16x32_f16 v[30:33], v[110:113], v[138:141], v[30:33]
	v_mfma_f32_16x16x32_f16 v[14:17], v[114:117], v[138:141], v[14:17]
	ds_read_b128 v[138:141], v161 offset:30720
	s_waitcnt lgkmcnt(7)
	v_mfma_f32_16x16x32_f16 v[164:167], v[118:121], v[142:145], v[164:167]
	v_mfma_f32_16x16x32_f16 v[62:65], v[122:125], v[142:145], v[62:65]
	ds_read_b128 v[142:145], v161 offset:32768
	s_waitcnt lgkmcnt(7)
	v_mfma_f32_16x16x32_f16 v[86:89], v[118:121], v[146:149], v[86:89]
	v_mfma_f32_16x16x32_f16 v[58:61], v[122:125], v[146:149], v[58:61]
	ds_read_b128 v[146:149], v161 offset:34816
	s_waitcnt lgkmcnt(7)
	v_mfma_f32_16x16x32_f16 v[96:99], v[118:121], v[150:153], v[96:99]
	v_mfma_f32_16x16x32_f16 v[54:57], v[122:125], v[150:153], v[54:57]
	ds_read_b128 v[150:153], v161 offset:36864
	s_waitcnt lgkmcnt(7)
	v_mfma_f32_16x16x32_f16 v[82:85], v[118:121], v[154:157], v[82:85]
	v_mfma_f32_16x16x32_f16 v[50:53], v[122:125], v[154:157], v[50:53]
	ds_read_b128 v[154:157], v161 offset:38912
	s_waitcnt lgkmcnt(0)
	s_barrier
	s_mov_b32 m0, s28
	s_nop 0
	global_load_lds_dwordx4 v104, s[38:39]
	s_mov_b32 m0, s29
	s_nop 0
	global_load_lds_dwordx4 v105, s[38:39]
	s_mov_b32 m0, s30
	s_nop 0
	global_load_lds_dwordx4 v106, s[38:39]
	s_mov_b32 m0, s31
	s_nop 0
	global_load_lds_dwordx4 v107, s[38:39]
	s_mov_b32 m0, s32
	s_nop 0
	global_load_lds_dwordx4 v108, s[38:39]
	s_mov_b32 m0, s33
	s_nop 0
	global_load_lds_dwordx4 v109, s[38:39]
	s_add_u32 s38, s38, 0x80
	s_addc_u32 s39, s39, 0
	s_waitcnt lgkmcnt(7)
	v_mfma_f32_16x16x32_f16 v[78:81], v[118:121], v[126:129], v[78:81]
	v_mfma_f32_16x16x32_f16 v[46:49], v[122:125], v[126:129], v[46:49]
	s_waitcnt lgkmcnt(6)
	v_mfma_f32_16x16x32_f16 v[74:77], v[118:121], v[130:133], v[74:77]
	v_mfma_f32_16x16x32_f16 v[42:45], v[122:125], v[130:133], v[42:45]
	s_waitcnt lgkmcnt(5)
	v_mfma_f32_16x16x32_f16 v[70:73], v[118:121], v[134:137], v[70:73]
	v_mfma_f32_16x16x32_f16 v[38:41], v[122:125], v[134:137], v[38:41]
	s_waitcnt lgkmcnt(4)
	v_mfma_f32_16x16x32_f16 v[66:69], v[118:121], v[138:141], v[66:69]
	v_mfma_f32_16x16x32_f16 v[34:37], v[122:125], v[138:141], v[34:37]
	s_waitcnt lgkmcnt(3)
	v_mfma_f32_16x16x32_f16 v[18:21], v[118:121], v[142:145], v[18:21]
	v_mfma_f32_16x16x32_f16 v[2:5], v[122:125], v[142:145], v[2:5]
	s_waitcnt lgkmcnt(2)
	v_mfma_f32_16x16x32_f16 v[26:29], v[118:121], v[146:149], v[26:29]
	v_mfma_f32_16x16x32_f16 v[10:13], v[122:125], v[146:149], v[10:13]
	s_waitcnt lgkmcnt(1)
	v_mfma_f32_16x16x32_f16 v[22:25], v[118:121], v[150:153], v[22:25]
	v_mfma_f32_16x16x32_f16 v[6:9], v[122:125], v[150:153], v[6:9]
	s_waitcnt lgkmcnt(0)
	v_mfma_f32_16x16x32_f16 v[30:33], v[118:121], v[154:157], v[30:33]
	v_mfma_f32_16x16x32_f16 v[14:17], v[122:125], v[154:157], v[14:17]
	s_waitcnt vmcnt(0)
	s_barrier
	ds_read_b128 v[110:113], v158 offset:0
	ds_read_b128 v[114:117], v158 offset:2048
	ds_read_b128 v[118:121], v159 offset:0
	ds_read_b128 v[122:125], v159 offset:2048
	ds_read_b128 v[126:129], v160 offset:16384
	ds_read_b128 v[130:133], v160 offset:18432
	ds_read_b128 v[134:137], v160 offset:20480
	ds_read_b128 v[138:141], v160 offset:22528
	ds_read_b128 v[142:145], v160 offset:24576
	ds_read_b128 v[146:149], v160 offset:26624
	ds_read_b128 v[150:153], v160 offset:28672
	ds_read_b128 v[154:157], v160 offset:30720
	s_waitcnt lgkmcnt(7)
	v_mfma_f32_16x16x32_f16 v[164:167], v[110:113], v[126:129], v[164:167]
	v_mfma_f32_16x16x32_f16 v[62:65], v[114:117], v[126:129], v[62:65]
	ds_read_b128 v[126:129], v160 offset:32768
	s_waitcnt lgkmcnt(7)
	v_mfma_f32_16x16x32_f16 v[86:89], v[110:113], v[130:133], v[86:89]
	v_mfma_f32_16x16x32_f16 v[58:61], v[114:117], v[130:133], v[58:61]
	ds_read_b128 v[130:133], v160 offset:34816
	s_waitcnt lgkmcnt(10)
	s_barrier
	s_mov_b32 m0, s24
	s_nop 0
	global_load_lds_dwordx4 v100, s[36:37]
	s_mov_b32 m0, s25
	s_nop 0
	global_load_lds_dwordx4 v101, s[36:37]
	s_mov_b32 m0, s26
	s_nop 0
	global_load_lds_dwordx4 v102, s[36:37]
	s_mov_b32 m0, s27
	s_nop 0
	global_load_lds_dwordx4 v103, s[36:37]
	s_add_u32 s36, s36, 0x80
	s_addc_u32 s37, s37, 0
	s_waitcnt lgkmcnt(7)
	v_mfma_f32_16x16x32_f16 v[96:99], v[110:113], v[134:137], v[96:99]
	v_mfma_f32_16x16x32_f16 v[54:57], v[114:117], v[134:137], v[54:57]
	ds_read_b128 v[134:137], v160 offset:36864
	s_waitcnt lgkmcnt(7)
	v_mfma_f32_16x16x32_f16 v[82:85], v[110:113], v[138:141], v[82:85]
	v_mfma_f32_16x16x32_f16 v[50:53], v[114:117], v[138:141], v[50:53]
	ds_read_b128 v[138:141], v160 offset:38912
	s_waitcnt lgkmcnt(7)
	v_mfma_f32_16x16x32_f16 v[78:81], v[110:113], v[142:145], v[78:81]
	v_mfma_f32_16x16x32_f16 v[46:49], v[114:117], v[142:145], v[46:49]
	ds_read_b128 v[142:145], v161 offset:16384
	s_waitcnt lgkmcnt(7)
	v_mfma_f32_16x16x32_f16 v[74:77], v[110:113], v[146:149], v[74:77]
	v_mfma_f32_16x16x32_f16 v[42:45], v[114:117], v[146:149], v[42:45]
	ds_read_b128 v[146:149], v161 offset:18432
	s_waitcnt lgkmcnt(7)
	v_mfma_f32_16x16x32_f16 v[70:73], v[110:113], v[150:153], v[70:73]
	v_mfma_f32_16x16x32_f16 v[38:41], v[114:117], v[150:153], v[38:41]
	ds_read_b128 v[150:153], v161 offset:20480
	s_waitcnt lgkmcnt(7)
	v_mfma_f32_16x16x32_f16 v[66:69], v[110:113], v[154:157], v[66:69]
	v_mfma_f32_16x16x32_f16 v[34:37], v[114:117], v[154:157], v[34:37]
	ds_read_b128 v[154:157], v161 offset:22528
	s_waitcnt lgkmcnt(7)
	v_mfma_f32_16x16x32_f16 v[18:21], v[110:113], v[126:129], v[18:21]
	v_mfma_f32_16x16x32_f16 v[2:5], v[114:117], v[126:129], v[2:5]
	ds_read_b128 v[126:129], v161 offset:24576
	s_waitcnt lgkmcnt(7)
	v_mfma_f32_16x16x32_f16 v[26:29], v[110:113], v[130:133], v[26:29]
	v_mfma_f32_16x16x32_f16 v[10:13], v[114:117], v[130:133], v[10:13]
	ds_read_b128 v[130:133], v161 offset:26624
	s_waitcnt lgkmcnt(7)
	v_mfma_f32_16x16x32_f16 v[22:25], v[110:113], v[134:137], v[22:25]
	v_mfma_f32_16x16x32_f16 v[6:9], v[114:117], v[134:137], v[6:9]
	ds_read_b128 v[134:137], v161 offset:28672
	s_waitcnt lgkmcnt(7)
	v_mfma_f32_16x16x32_f16 v[30:33], v[110:113], v[138:141], v[30:33]
	v_mfma_f32_16x16x32_f16 v[14:17], v[114:117], v[138:141], v[14:17]
	ds_read_b128 v[138:141], v161 offset:30720
	s_waitcnt lgkmcnt(7)
	v_mfma_f32_16x16x32_f16 v[164:167], v[118:121], v[142:145], v[164:167]
	v_mfma_f32_16x16x32_f16 v[62:65], v[122:125], v[142:145], v[62:65]
	ds_read_b128 v[142:145], v161 offset:32768
	s_waitcnt lgkmcnt(7)
	v_mfma_f32_16x16x32_f16 v[86:89], v[118:121], v[146:149], v[86:89]
	v_mfma_f32_16x16x32_f16 v[58:61], v[122:125], v[146:149], v[58:61]
	ds_read_b128 v[146:149], v161 offset:34816
	s_waitcnt lgkmcnt(7)
	v_mfma_f32_16x16x32_f16 v[96:99], v[118:121], v[150:153], v[96:99]
	v_mfma_f32_16x16x32_f16 v[54:57], v[122:125], v[150:153], v[54:57]
	ds_read_b128 v[150:153], v161 offset:36864
	s_waitcnt lgkmcnt(7)
	v_mfma_f32_16x16x32_f16 v[82:85], v[118:121], v[154:157], v[82:85]
	v_mfma_f32_16x16x32_f16 v[50:53], v[122:125], v[154:157], v[50:53]
	ds_read_b128 v[154:157], v161 offset:38912
	s_waitcnt lgkmcnt(0)
	s_barrier
	s_mov_b32 m0, s28
	s_nop 0
	global_load_lds_dwordx4 v104, s[38:39]
	s_mov_b32 m0, s29
	s_nop 0
	global_load_lds_dwordx4 v105, s[38:39]
	s_mov_b32 m0, s30
	s_nop 0
	global_load_lds_dwordx4 v106, s[38:39]
	s_mov_b32 m0, s31
	s_nop 0
	global_load_lds_dwordx4 v107, s[38:39]
	s_mov_b32 m0, s32
	s_nop 0
	global_load_lds_dwordx4 v108, s[38:39]
	s_mov_b32 m0, s33
	s_nop 0
	global_load_lds_dwordx4 v109, s[38:39]
	s_add_u32 s38, s38, 0x80
	s_addc_u32 s39, s39, 0
	s_waitcnt lgkmcnt(7)
	v_mfma_f32_16x16x32_f16 v[78:81], v[118:121], v[126:129], v[78:81]
	v_mfma_f32_16x16x32_f16 v[46:49], v[122:125], v[126:129], v[46:49]
	s_waitcnt lgkmcnt(6)
	v_mfma_f32_16x16x32_f16 v[74:77], v[118:121], v[130:133], v[74:77]
	v_mfma_f32_16x16x32_f16 v[42:45], v[122:125], v[130:133], v[42:45]
	s_waitcnt lgkmcnt(5)
	v_mfma_f32_16x16x32_f16 v[70:73], v[118:121], v[134:137], v[70:73]
	v_mfma_f32_16x16x32_f16 v[38:41], v[122:125], v[134:137], v[38:41]
	s_waitcnt lgkmcnt(4)
	v_mfma_f32_16x16x32_f16 v[66:69], v[118:121], v[138:141], v[66:69]
	v_mfma_f32_16x16x32_f16 v[34:37], v[122:125], v[138:141], v[34:37]
	s_waitcnt lgkmcnt(3)
	v_mfma_f32_16x16x32_f16 v[18:21], v[118:121], v[142:145], v[18:21]
	v_mfma_f32_16x16x32_f16 v[2:5], v[122:125], v[142:145], v[2:5]
	s_waitcnt lgkmcnt(2)
	v_mfma_f32_16x16x32_f16 v[26:29], v[118:121], v[146:149], v[26:29]
	v_mfma_f32_16x16x32_f16 v[10:13], v[122:125], v[146:149], v[10:13]
	s_waitcnt lgkmcnt(1)
	v_mfma_f32_16x16x32_f16 v[22:25], v[118:121], v[150:153], v[22:25]
	v_mfma_f32_16x16x32_f16 v[6:9], v[122:125], v[150:153], v[6:9]
	s_waitcnt lgkmcnt(0)
	v_mfma_f32_16x16x32_f16 v[30:33], v[118:121], v[154:157], v[30:33]
	v_mfma_f32_16x16x32_f16 v[14:17], v[122:125], v[154:157], v[14:17]
	s_waitcnt vmcnt(0)
	s_barrier
	ds_read_b128 v[110:113], v158 offset:0
	ds_read_b128 v[114:117], v158 offset:2048
	ds_read_b128 v[118:121], v159 offset:0
	ds_read_b128 v[122:125], v159 offset:2048
	ds_read_b128 v[126:129], v160 offset:16384
	ds_read_b128 v[130:133], v160 offset:18432
	ds_read_b128 v[134:137], v160 offset:20480
	ds_read_b128 v[138:141], v160 offset:22528
	ds_read_b128 v[142:145], v160 offset:24576
	ds_read_b128 v[146:149], v160 offset:26624
	ds_read_b128 v[150:153], v160 offset:28672
	ds_read_b128 v[154:157], v160 offset:30720
	s_waitcnt lgkmcnt(7)
	v_mfma_f32_16x16x32_f16 v[164:167], v[110:113], v[126:129], v[164:167]
	v_mfma_f32_16x16x32_f16 v[62:65], v[114:117], v[126:129], v[62:65]
	ds_read_b128 v[126:129], v160 offset:32768
	s_waitcnt lgkmcnt(7)
	v_mfma_f32_16x16x32_f16 v[86:89], v[110:113], v[130:133], v[86:89]
	v_mfma_f32_16x16x32_f16 v[58:61], v[114:117], v[130:133], v[58:61]
	ds_read_b128 v[130:133], v160 offset:34816
	s_waitcnt lgkmcnt(10)
	s_barrier
	s_mov_b32 m0, s24
	s_nop 0
	global_load_lds_dwordx4 v100, s[36:37]
	s_mov_b32 m0, s25
	s_nop 0
	global_load_lds_dwordx4 v101, s[36:37]
	s_mov_b32 m0, s26
	s_nop 0
	global_load_lds_dwordx4 v102, s[36:37]
	s_mov_b32 m0, s27
	s_nop 0
	global_load_lds_dwordx4 v103, s[36:37]
	s_add_u32 s36, s36, 0x80
	s_addc_u32 s37, s37, 0
	s_waitcnt lgkmcnt(7)
	v_mfma_f32_16x16x32_f16 v[96:99], v[110:113], v[134:137], v[96:99]
	v_mfma_f32_16x16x32_f16 v[54:57], v[114:117], v[134:137], v[54:57]
	ds_read_b128 v[134:137], v160 offset:36864
	s_waitcnt lgkmcnt(7)
	v_mfma_f32_16x16x32_f16 v[82:85], v[110:113], v[138:141], v[82:85]
	v_mfma_f32_16x16x32_f16 v[50:53], v[114:117], v[138:141], v[50:53]
	ds_read_b128 v[138:141], v160 offset:38912
	s_waitcnt lgkmcnt(7)
	v_mfma_f32_16x16x32_f16 v[78:81], v[110:113], v[142:145], v[78:81]
	v_mfma_f32_16x16x32_f16 v[46:49], v[114:117], v[142:145], v[46:49]
	ds_read_b128 v[142:145], v161 offset:16384
	s_waitcnt lgkmcnt(7)
	v_mfma_f32_16x16x32_f16 v[74:77], v[110:113], v[146:149], v[74:77]
	v_mfma_f32_16x16x32_f16 v[42:45], v[114:117], v[146:149], v[42:45]
	ds_read_b128 v[146:149], v161 offset:18432
	s_waitcnt lgkmcnt(7)
	v_mfma_f32_16x16x32_f16 v[70:73], v[110:113], v[150:153], v[70:73]
	v_mfma_f32_16x16x32_f16 v[38:41], v[114:117], v[150:153], v[38:41]
	ds_read_b128 v[150:153], v161 offset:20480
	s_waitcnt lgkmcnt(7)
	v_mfma_f32_16x16x32_f16 v[66:69], v[110:113], v[154:157], v[66:69]
	v_mfma_f32_16x16x32_f16 v[34:37], v[114:117], v[154:157], v[34:37]
	ds_read_b128 v[154:157], v161 offset:22528
	s_waitcnt lgkmcnt(7)
	v_mfma_f32_16x16x32_f16 v[18:21], v[110:113], v[126:129], v[18:21]
	v_mfma_f32_16x16x32_f16 v[2:5], v[114:117], v[126:129], v[2:5]
	ds_read_b128 v[126:129], v161 offset:24576
	s_waitcnt lgkmcnt(7)
	v_mfma_f32_16x16x32_f16 v[26:29], v[110:113], v[130:133], v[26:29]
	v_mfma_f32_16x16x32_f16 v[10:13], v[114:117], v[130:133], v[10:13]
	ds_read_b128 v[130:133], v161 offset:26624
	s_waitcnt lgkmcnt(7)
	v_mfma_f32_16x16x32_f16 v[22:25], v[110:113], v[134:137], v[22:25]
	v_mfma_f32_16x16x32_f16 v[6:9], v[114:117], v[134:137], v[6:9]
	ds_read_b128 v[134:137], v161 offset:28672
	s_waitcnt lgkmcnt(7)
	v_mfma_f32_16x16x32_f16 v[30:33], v[110:113], v[138:141], v[30:33]
	v_mfma_f32_16x16x32_f16 v[14:17], v[114:117], v[138:141], v[14:17]
	ds_read_b128 v[138:141], v161 offset:30720
	s_waitcnt lgkmcnt(7)
	v_mfma_f32_16x16x32_f16 v[164:167], v[118:121], v[142:145], v[164:167]
	v_mfma_f32_16x16x32_f16 v[62:65], v[122:125], v[142:145], v[62:65]
	ds_read_b128 v[142:145], v161 offset:32768
	s_waitcnt lgkmcnt(7)
	v_mfma_f32_16x16x32_f16 v[86:89], v[118:121], v[146:149], v[86:89]
	v_mfma_f32_16x16x32_f16 v[58:61], v[122:125], v[146:149], v[58:61]
	ds_read_b128 v[146:149], v161 offset:34816
	s_waitcnt lgkmcnt(7)
	v_mfma_f32_16x16x32_f16 v[96:99], v[118:121], v[150:153], v[96:99]
	v_mfma_f32_16x16x32_f16 v[54:57], v[122:125], v[150:153], v[54:57]
	ds_read_b128 v[150:153], v161 offset:36864
	s_waitcnt lgkmcnt(7)
	v_mfma_f32_16x16x32_f16 v[82:85], v[118:121], v[154:157], v[82:85]
	v_mfma_f32_16x16x32_f16 v[50:53], v[122:125], v[154:157], v[50:53]
	ds_read_b128 v[154:157], v161 offset:38912
	s_waitcnt lgkmcnt(0)
	s_barrier
	s_mov_b32 m0, s28
	s_nop 0
	global_load_lds_dwordx4 v104, s[38:39]
	s_mov_b32 m0, s29
	s_nop 0
	global_load_lds_dwordx4 v105, s[38:39]
	s_mov_b32 m0, s30
	s_nop 0
	global_load_lds_dwordx4 v106, s[38:39]
	s_mov_b32 m0, s31
	s_nop 0
	global_load_lds_dwordx4 v107, s[38:39]
	s_mov_b32 m0, s32
	s_nop 0
	global_load_lds_dwordx4 v108, s[38:39]
	s_mov_b32 m0, s33
	s_nop 0
	global_load_lds_dwordx4 v109, s[38:39]
	s_add_u32 s38, s38, 0x80
	s_addc_u32 s39, s39, 0
	s_waitcnt lgkmcnt(7)
	v_mfma_f32_16x16x32_f16 v[78:81], v[118:121], v[126:129], v[78:81]
	v_mfma_f32_16x16x32_f16 v[46:49], v[122:125], v[126:129], v[46:49]
	s_waitcnt lgkmcnt(6)
	v_mfma_f32_16x16x32_f16 v[74:77], v[118:121], v[130:133], v[74:77]
	v_mfma_f32_16x16x32_f16 v[42:45], v[122:125], v[130:133], v[42:45]
	s_waitcnt lgkmcnt(5)
	v_mfma_f32_16x16x32_f16 v[70:73], v[118:121], v[134:137], v[70:73]
	v_mfma_f32_16x16x32_f16 v[38:41], v[122:125], v[134:137], v[38:41]
	s_waitcnt lgkmcnt(4)
	v_mfma_f32_16x16x32_f16 v[66:69], v[118:121], v[138:141], v[66:69]
	v_mfma_f32_16x16x32_f16 v[34:37], v[122:125], v[138:141], v[34:37]
	s_waitcnt lgkmcnt(3)
	v_mfma_f32_16x16x32_f16 v[18:21], v[118:121], v[142:145], v[18:21]
	v_mfma_f32_16x16x32_f16 v[2:5], v[122:125], v[142:145], v[2:5]
	s_waitcnt lgkmcnt(2)
	v_mfma_f32_16x16x32_f16 v[26:29], v[118:121], v[146:149], v[26:29]
	v_mfma_f32_16x16x32_f16 v[10:13], v[122:125], v[146:149], v[10:13]
	s_waitcnt lgkmcnt(1)
	v_mfma_f32_16x16x32_f16 v[22:25], v[118:121], v[150:153], v[22:25]
	v_mfma_f32_16x16x32_f16 v[6:9], v[122:125], v[150:153], v[6:9]
	s_waitcnt lgkmcnt(0)
	v_mfma_f32_16x16x32_f16 v[30:33], v[118:121], v[154:157], v[30:33]
	v_mfma_f32_16x16x32_f16 v[14:17], v[122:125], v[154:157], v[14:17]
	s_waitcnt vmcnt(0)
	s_barrier
	ds_read_b128 v[110:113], v158 offset:0
	ds_read_b128 v[114:117], v158 offset:2048
	ds_read_b128 v[118:121], v159 offset:0
	ds_read_b128 v[122:125], v159 offset:2048
	ds_read_b128 v[126:129], v160 offset:16384
	ds_read_b128 v[130:133], v160 offset:18432
	ds_read_b128 v[134:137], v160 offset:20480
	ds_read_b128 v[138:141], v160 offset:22528
	ds_read_b128 v[142:145], v160 offset:24576
	ds_read_b128 v[146:149], v160 offset:26624
	ds_read_b128 v[150:153], v160 offset:28672
	ds_read_b128 v[154:157], v160 offset:30720
	s_waitcnt lgkmcnt(7)
	v_mfma_f32_16x16x32_f16 v[164:167], v[110:113], v[126:129], v[164:167]
	v_mfma_f32_16x16x32_f16 v[62:65], v[114:117], v[126:129], v[62:65]
	ds_read_b128 v[126:129], v160 offset:32768
	s_waitcnt lgkmcnt(7)
	v_mfma_f32_16x16x32_f16 v[86:89], v[110:113], v[130:133], v[86:89]
	v_mfma_f32_16x16x32_f16 v[58:61], v[114:117], v[130:133], v[58:61]
	ds_read_b128 v[130:133], v160 offset:34816
	s_waitcnt lgkmcnt(7)
	v_mfma_f32_16x16x32_f16 v[96:99], v[110:113], v[134:137], v[96:99]
	v_mfma_f32_16x16x32_f16 v[54:57], v[114:117], v[134:137], v[54:57]
	ds_read_b128 v[134:137], v160 offset:36864
	s_waitcnt lgkmcnt(7)
	v_mfma_f32_16x16x32_f16 v[82:85], v[110:113], v[138:141], v[82:85]
	v_mfma_f32_16x16x32_f16 v[50:53], v[114:117], v[138:141], v[50:53]
	ds_read_b128 v[138:141], v160 offset:38912
	s_waitcnt lgkmcnt(7)
	v_mfma_f32_16x16x32_f16 v[78:81], v[110:113], v[142:145], v[78:81]
	v_mfma_f32_16x16x32_f16 v[46:49], v[114:117], v[142:145], v[46:49]
	ds_read_b128 v[142:145], v161 offset:16384
	s_waitcnt lgkmcnt(7)
	v_mfma_f32_16x16x32_f16 v[74:77], v[110:113], v[146:149], v[74:77]
	v_mfma_f32_16x16x32_f16 v[42:45], v[114:117], v[146:149], v[42:45]
	ds_read_b128 v[146:149], v161 offset:18432
	s_waitcnt lgkmcnt(7)
	v_mfma_f32_16x16x32_f16 v[70:73], v[110:113], v[150:153], v[70:73]
	v_mfma_f32_16x16x32_f16 v[38:41], v[114:117], v[150:153], v[38:41]
	ds_read_b128 v[150:153], v161 offset:20480
	s_waitcnt lgkmcnt(7)
	v_mfma_f32_16x16x32_f16 v[66:69], v[110:113], v[154:157], v[66:69]
	v_mfma_f32_16x16x32_f16 v[34:37], v[114:117], v[154:157], v[34:37]
	ds_read_b128 v[154:157], v161 offset:22528
	s_waitcnt lgkmcnt(7)
	v_mfma_f32_16x16x32_f16 v[18:21], v[110:113], v[126:129], v[18:21]
	v_mfma_f32_16x16x32_f16 v[2:5], v[114:117], v[126:129], v[2:5]
	ds_read_b128 v[126:129], v161 offset:24576
	s_waitcnt lgkmcnt(7)
	v_mfma_f32_16x16x32_f16 v[26:29], v[110:113], v[130:133], v[26:29]
	v_mfma_f32_16x16x32_f16 v[10:13], v[114:117], v[130:133], v[10:13]
	ds_read_b128 v[130:133], v161 offset:26624
	s_waitcnt lgkmcnt(7)
	v_mfma_f32_16x16x32_f16 v[22:25], v[110:113], v[134:137], v[22:25]
	v_mfma_f32_16x16x32_f16 v[6:9], v[114:117], v[134:137], v[6:9]
	ds_read_b128 v[134:137], v161 offset:28672
	s_waitcnt lgkmcnt(7)
	v_mfma_f32_16x16x32_f16 v[30:33], v[110:113], v[138:141], v[30:33]
	v_mfma_f32_16x16x32_f16 v[14:17], v[114:117], v[138:141], v[14:17]
	ds_read_b128 v[138:141], v161 offset:30720
	s_waitcnt lgkmcnt(7)
	v_mfma_f32_16x16x32_f16 v[164:167], v[118:121], v[142:145], v[164:167]
	v_mfma_f32_16x16x32_f16 v[62:65], v[122:125], v[142:145], v[62:65]
	ds_read_b128 v[142:145], v161 offset:32768
	s_waitcnt lgkmcnt(7)
	v_mfma_f32_16x16x32_f16 v[86:89], v[118:121], v[146:149], v[86:89]
	v_mfma_f32_16x16x32_f16 v[58:61], v[122:125], v[146:149], v[58:61]
	ds_read_b128 v[146:149], v161 offset:34816
	s_waitcnt lgkmcnt(7)
	v_mfma_f32_16x16x32_f16 v[96:99], v[118:121], v[150:153], v[96:99]
	v_mfma_f32_16x16x32_f16 v[54:57], v[122:125], v[150:153], v[54:57]
	ds_read_b128 v[150:153], v161 offset:36864
	s_waitcnt lgkmcnt(7)
	v_mfma_f32_16x16x32_f16 v[82:85], v[118:121], v[154:157], v[82:85]
	v_mfma_f32_16x16x32_f16 v[50:53], v[122:125], v[154:157], v[50:53]
	ds_read_b128 v[154:157], v161 offset:38912
	s_waitcnt lgkmcnt(0)
	s_barrier
	s_waitcnt lgkmcnt(7)
	v_mfma_f32_16x16x32_f16 v[78:81], v[118:121], v[126:129], v[78:81]
	v_mfma_f32_16x16x32_f16 v[46:49], v[122:125], v[126:129], v[46:49]
	s_waitcnt lgkmcnt(6)
	v_mfma_f32_16x16x32_f16 v[74:77], v[118:121], v[130:133], v[74:77]
	v_mfma_f32_16x16x32_f16 v[42:45], v[122:125], v[130:133], v[42:45]
	s_waitcnt lgkmcnt(5)
	v_mfma_f32_16x16x32_f16 v[70:73], v[118:121], v[134:137], v[70:73]
	v_mfma_f32_16x16x32_f16 v[38:41], v[122:125], v[134:137], v[38:41]
	s_waitcnt lgkmcnt(4)
	v_mfma_f32_16x16x32_f16 v[66:69], v[118:121], v[138:141], v[66:69]
	v_mfma_f32_16x16x32_f16 v[34:37], v[122:125], v[138:141], v[34:37]
	s_waitcnt lgkmcnt(3)
	v_mfma_f32_16x16x32_f16 v[18:21], v[118:121], v[142:145], v[18:21]
	v_mfma_f32_16x16x32_f16 v[2:5], v[122:125], v[142:145], v[2:5]
	s_waitcnt lgkmcnt(2)
	v_mfma_f32_16x16x32_f16 v[26:29], v[118:121], v[146:149], v[26:29]
	v_mfma_f32_16x16x32_f16 v[10:13], v[122:125], v[146:149], v[10:13]
	s_waitcnt lgkmcnt(1)
	v_mfma_f32_16x16x32_f16 v[22:25], v[118:121], v[150:153], v[22:25]
	v_mfma_f32_16x16x32_f16 v[6:9], v[122:125], v[150:153], v[6:9]
	s_waitcnt lgkmcnt(0)
	v_mfma_f32_16x16x32_f16 v[30:33], v[118:121], v[154:157], v[30:33]
	v_mfma_f32_16x16x32_f16 v[14:17], v[122:125], v[154:157], v[14:17]
	s_nop 15
	s_nop 15
	s_movk_i32 s2, 0xfc
	v_cmp_gt_u32_e32 vcc, s2, v0
	s_mov_b32 s2, 0x12492493
	s_movk_i32 s4, 0x380
	s_movk_i32 s12, 0x110
	v_cmp_gt_u32_e64 s[4:5], s4, v0
	v_lshrrev_b32_e32 v93, 1, v0
	v_cndmask_b32_e32 v94, 0, v93, vcc
	s_nop 5
	v_cvt_f16_f32_e32 v86, v86
	s_nop 5
	v_cvt_f16_f32_e32 v54, v54
	v_cvt_f16_f32_e32 v82, v82
	v_cvt_f16_f32_e32 v50, v50
	s_nop 5
	v_cvt_f16_f32_e32 v78, v78
	v_mul_i32_i24_e32 v102, 0xffffffc2, v92
	v_mul_u32_u24_e32 v101, 0x110, v91
	v_lshlrev_b32_e32 v91, 6, v92
	v_add3_u32 v91, v91, v102, v101
	ds_write_b16 v91, v86 offset:32
	v_cvt_f16_f32_e32 v86, v87
	v_cvt_f16_f32_e32 v74, v74
	v_cvt_f16_f32_e32 v102, v165
	ds_write_b16 v91, v86 offset:304
	v_cvt_f16_f32_e32 v86, v88
	s_nop 2
	v_cvt_f16_f32_e32 v34, v34
	ds_write_b16 v91, v82 offset:96
	ds_write_b16 v91, v86 offset:576
	v_cvt_f16_f32_e32 v86, v89
	v_cvt_f16_f32_e32 v38, v38
	ds_write_b16 v91, v34 offset:4576
	ds_write_b16 v91, v86 offset:848
	v_cvt_f16_f32_e32 v86, v96
	s_nop 1
	v_cvt_f16_f32_e32 v62, v62
	v_cvt_f16_f32_e32 v34, v35
	s_nop 0
	v_cvt_f16_f32_e32 v58, v58
	ds_write_b16 v91, v38 offset:4544
	v_cvt_f16_f32_e32 v38, v39
	s_nop 1
	v_cvt_f16_f32_e32 v46, v46
	ds_write_b16 v91, v86 offset:64
	v_cvt_f16_f32_e32 v86, v97
	s_nop 0
	v_cvt_f16_f32_e32 v42, v42
	v_cvt_f16_f32_e32 v82, v83
	ds_write_b16 v91, v78 offset:128
	s_nop 1
	v_cvt_f16_f32_e32 v70, v70
	v_cvt_f16_f32_e32 v78, v79
	ds_write_b16 v91, v74 offset:160
	v_cvt_f16_f32_e32 v74, v75
	s_nop 0
	v_cvt_f16_f32_e32 v66, v66
	ds_write_b16 v91, v70 offset:192
	v_cvt_f16_f32_e32 v70, v71
	ds_write_b16 v91, v62 offset:4352
	ds_write_b16 v91, v66 offset:224
	v_cvt_f16_f32_e32 v66, v67
	v_cvt_f16_f32_e32 v62, v63
	ds_write_b16 v91, v58 offset:4384
	v_cvt_f16_f32_e32 v58, v59
	ds_write_b16 v91, v54 offset:4416
	v_cvt_f16_f32_e32 v54, v55
	ds_write_b16 v91, v50 offset:4448
	v_cvt_f16_f32_e32 v50, v51
	ds_write_b16 v91, v46 offset:4480
	v_cvt_f16_f32_e32 v46, v47
	ds_write_b16 v91, v42 offset:4512
	v_cvt_f16_f32_e32 v42, v43
	ds_write_b16 v91, v34 offset:4848
	v_cvt_f16_f32_e32 v34, v36
	ds_write_b16 v91, v38 offset:4816
	v_cvt_f16_f32_e32 v38, v40
	ds_write_b16 v91, v102 offset:272
	v_cvt_f16_f32_e32 v102, v166
	ds_write_b16 v91, v86 offset:336
	v_cvt_f16_f32_e32 v86, v98
	ds_write_b16 v91, v82 offset:368
	v_cvt_f16_f32_e32 v82, v84
	ds_write_b16 v91, v78 offset:400
	v_cvt_f16_f32_e32 v78, v80
	ds_write_b16 v91, v74 offset:432
	v_cvt_f16_f32_e32 v74, v76
	ds_write_b16 v91, v70 offset:464
	v_cvt_f16_f32_e32 v70, v72
	ds_write_b16 v91, v66 offset:496
	v_cvt_f16_f32_e32 v66, v68
	ds_write_b16 v91, v62 offset:4624
	v_cvt_f16_f32_e32 v62, v64
	ds_write_b16 v91, v58 offset:4656
	v_cvt_f16_f32_e32 v58, v60
	ds_write_b16 v91, v54 offset:4688
	v_cvt_f16_f32_e32 v54, v56
	ds_write_b16 v91, v50 offset:4720
	v_cvt_f16_f32_e32 v50, v52
	ds_write_b16 v91, v46 offset:4752
	v_cvt_f16_f32_e32 v46, v48
	ds_write_b16 v91, v42 offset:4784
	v_cvt_f16_f32_e32 v42, v44
	ds_write_b16 v91, v34 offset:5120
	v_cvt_f16_f32_e32 v34, v37
	ds_write_b16 v91, v38 offset:5088
	v_cvt_f16_f32_e32 v38, v41
	v_cvt_f16_f32_e32 v103, v164
	ds_write_b16 v91, v102 offset:544
	v_cvt_f16_f32_e32 v102, v167
	ds_write_b16 v91, v86 offset:608
	v_cvt_f16_f32_e32 v86, v99
	ds_write_b16 v91, v82 offset:640
	v_cvt_f16_f32_e32 v82, v85
	ds_write_b16 v91, v78 offset:672
	v_cvt_f16_f32_e32 v78, v81
	ds_write_b16 v91, v74 offset:704
	v_cvt_f16_f32_e32 v74, v77
	ds_write_b16 v91, v70 offset:736
	v_cvt_f16_f32_e32 v70, v73
	ds_write_b16 v91, v66 offset:768
	v_cvt_f16_f32_e32 v66, v69
	ds_write_b16 v91, v62 offset:4896
	v_cvt_f16_f32_e32 v62, v65
	ds_write_b16 v91, v58 offset:4928
	v_cvt_f16_f32_e32 v58, v61
	ds_write_b16 v91, v54 offset:4960
	v_cvt_f16_f32_e32 v54, v57
	ds_write_b16 v91, v50 offset:4992
	v_cvt_f16_f32_e32 v50, v53
	ds_write_b16 v91, v46 offset:5024
	v_cvt_f16_f32_e32 v46, v49
	ds_write_b16 v91, v42 offset:5056
	v_cvt_f16_f32_e32 v42, v45
	ds_write_b16 v91, v34 offset:5392
	v_min_u32_e32 v34, 8, v92
	v_mul_hi_u32 v100, v94, s2
	ds_write_b16 v91, v38 offset:5360
	v_cmp_gt_u32_e64 s[2:3], 9, v92
	v_mul_u32_u24_e32 v39, 14, v34
	v_and_b32_e32 v40, 48, v0
	v_lshlrev_b32_e32 v38, 2, v92
	ds_write_b16 v91, v103
	ds_write_b16 v91, v102 offset:816
	ds_write_b16 v91, v86 offset:880
	ds_write_b16 v91, v82 offset:912
	ds_write_b16 v91, v78 offset:944
	ds_write_b16 v91, v74 offset:976
	ds_write_b16 v91, v70 offset:1008
	ds_write_b16 v91, v66 offset:1040
	ds_write_b16 v91, v62 offset:5168
	ds_write_b16 v91, v58 offset:5200
	ds_write_b16 v91, v54 offset:5232
	ds_write_b16 v91, v50 offset:5264
	ds_write_b16 v91, v46 offset:5296
	ds_write_b16 v91, v42 offset:5328
	s_waitcnt lgkmcnt(0)
	s_barrier
	s_and_saveexec_b64 s[6:7], s[4:5]
	s_cbranch_execz .LBB1_9
	v_add_u32_e32 v34, v1, v39
	v_mad_u32_u24 v41, v34, s12, v40
	ds_read_b128 v[34:37], v41
	ds_read_b128 v[42:45], v41 offset:64
	ds_read_b128 v[46:49], v41 offset:128
	ds_read_b128 v[50:53], v41 offset:192
	v_cmp_ne_u32_e64 s[4:5], 3, v90
	v_mul_u32_u24_e32 v41, 9, v1
	s_and_b64 s[12:13], s[4:5], s[2:3]
	s_waitcnt lgkmcnt(1)
	v_mfma_f32_16x16x32_f16 v[34:37], v[34:37], v[46:49], 0
	s_waitcnt lgkmcnt(0)
	v_mfma_f32_16x16x32_f16 v[34:37], v[42:45], v[50:53], v[34:37]
	s_and_saveexec_b64 s[4:5], s[12:13]
	v_add_u32_e32 v42, v95, v41
	s_nop 5
	v_mul_f32_e32 v34, 0x3e000000, v34
	v_mad_u32_u24 v42, v42, 48, v38
	ds_write_b32 v42, v34 offset:35328
	s_or_b64 exec, exec, s[4:5]
	v_or_b32_e32 v34, 1, v95
	v_cmp_gt_u32_e64 s[4:5], 9, v34
	s_and_b64 s[12:13], s[4:5], s[2:3]
	s_and_saveexec_b64 s[4:5], s[12:13]
	v_add_u32_e32 v34, v34, v41
	v_mul_f32_e32 v35, 0x3e000000, v35
	v_mad_u32_u24 v34, v34, 48, v38
	ds_write_b32 v34, v35 offset:35328
	s_or_b64 exec, exec, s[4:5]
	v_or_b32_e32 v34, 2, v95
	v_cmp_gt_u32_e64 s[4:5], 9, v34
	s_and_b64 s[12:13], s[4:5], s[2:3]
	s_and_saveexec_b64 s[4:5], s[12:13]
	v_add_u32_e32 v34, v34, v41
	v_mul_f32_e32 v35, 0x3e000000, v36
	v_mad_u32_u24 v34, v34, 48, v38
	ds_write_b32 v34, v35 offset:35328
	s_or_b64 exec, exec, s[4:5]
	v_or_b32_e32 v34, 3, v95
	v_cmp_gt_u32_e64 s[4:5], 9, v34
	s_and_b64 s[4:5], s[4:5], s[2:3]
	s_and_b64 exec, exec, s[4:5]
	v_add_u32_e32 v34, v34, v41
	v_mul_f32_e32 v35, 0x3e000000, v37
	v_mad_u32_u24 v34, v34, 48, v38
	ds_write_b32 v34, v35 offset:35328
